# speedup vs baseline: 1.0057x; 1.0021x over previous
.LBB5_2:
	s_lshl_b32 s3, s3, 7
	s_lshl_b32 s16, s2, 7
	v_lshrrev_b32_e32 v1, 1, v0
	v_mov_b32_e32 v65, 0
	v_and_b32_e32 v82, 15, v0
	v_and_b32_e32 v1, 64, v1
	s_cmp_lt_i32 s18, 32
	v_mov_b32_e32 v64, v65
	v_mov_b32_e32 v63, v65
	v_mov_b32_e32 v62, v65
	v_mov_b32_e32 v61, v65
	v_mov_b32_e32 v60, v65
	v_mov_b32_e32 v59, v65
	v_mov_b32_e32 v58, v65
	v_mov_b32_e32 v57, v65
	v_mov_b32_e32 v56, v65
	v_mov_b32_e32 v55, v65
	v_mov_b32_e32 v54, v65
	v_mov_b32_e32 v53, v65
	v_mov_b32_e32 v52, v65
	v_mov_b32_e32 v51, v65
	v_mov_b32_e32 v50, v65
	v_mov_b32_e32 v49, v65
	v_mov_b32_e32 v48, v65
	v_mov_b32_e32 v47, v65
	v_mov_b32_e32 v46, v65
	v_mov_b32_e32 v45, v65
	v_mov_b32_e32 v44, v65
	v_mov_b32_e32 v43, v65
	v_mov_b32_e32 v42, v65
	v_mov_b32_e32 v41, v65
	v_mov_b32_e32 v40, v65
	v_mov_b32_e32 v39, v65
	v_mov_b32_e32 v38, v65
	v_mov_b32_e32 v37, v65
	v_mov_b32_e32 v36, v65
	v_mov_b32_e32 v35, v65
	v_mov_b32_e32 v34, v65
	v_mov_b32_e32 v33, v65
	v_mov_b32_e32 v32, v65
	v_mov_b32_e32 v31, v65
	v_mov_b32_e32 v30, v65
	v_mov_b32_e32 v29, v65
	v_mov_b32_e32 v28, v65
	v_mov_b32_e32 v27, v65
	v_mov_b32_e32 v26, v65
	v_mov_b32_e32 v25, v65
	v_mov_b32_e32 v24, v65
	v_mov_b32_e32 v23, v65
	v_mov_b32_e32 v22, v65
	v_mov_b32_e32 v21, v65
	v_mov_b32_e32 v20, v65
	v_mov_b32_e32 v19, v65
	v_mov_b32_e32 v18, v65
	v_mov_b32_e32 v17, v65
	v_mov_b32_e32 v16, v65
	v_mov_b32_e32 v15, v65
	v_mov_b32_e32 v14, v65
	v_mov_b32_e32 v13, v65
	v_mov_b32_e32 v12, v65
	v_mov_b32_e32 v11, v65
	v_mov_b32_e32 v10, v65
	v_mov_b32_e32 v9, v65
	v_mov_b32_e32 v8, v65
	v_mov_b32_e32 v7, v65
	v_mov_b32_e32 v6, v65
	v_mov_b32_e32 v5, v65
	v_mov_b32_e32 v4, v65
	v_mov_b32_e32 v3, v65
	v_mov_b32_e32 v2, v65
	s_cbranch_scc1 .LBB5_5
	s_mov_b32 s49, 0
	s_load_dword s36, s[0:1], 0x10
	s_load_dwordx4 s[28:31], s[0:1], 0x0
	s_load_dwordx4 s[32:35], s[0:1], 0x30
	s_load_dwordx2 s[46:47], s[0:1], 0x40
	s_mov_b32 s37, s18
	s_lshr_b32 s45, s18, 6
	s_mul_i32 s48, s49, s45
	s_lshl_b32 s48, s48, 7
	v_lshrrev_b32_e32 v98, 6, v0
	v_lshlrev_b32_e32 v98, 10, v98
	v_lshrrev_b32_e32 v222, 3, v0
	v_readfirstlane_b32 s44, v98
	v_and_b32_e32 v223, 7, v0
	v_and_b32_e32 v98, 7, v222
	v_xor_b32_e32 v223, v223, v98
	v_lshlrev_b32_e32 v223, 4, v223
	s_waitcnt lgkmcnt(0)
	s_lshl_b32 s38, s36, 6
	s_lshl_b32 s39, s36, 7
	s_add_u32 s40, s38, s39
	s_lshl_b32 s41, s37, 6
	s_lshl_b32 s42, s37, 7
	s_add_u32 s43, s41, s42
	s_mul_i32 s54, s3, s36
	s_lshl_b32 s54, s54, 1
	s_add_u32 s54, s54, s48
	s_add_u32 s28, s28, s54
	s_addc_u32 s29, s29, 0
	s_add_u32 s30, s30, s54
	s_addc_u32 s31, s31, 0
	s_mul_i32 s54, s49, s46
	s_mul_i32 s55, s16, s37
	s_add_u32 s54, s54, s55
	s_lshl_b32 s54, s54, 1
	s_add_u32 s54, s54, s48
	s_add_u32 s32, s32, s54
	s_addc_u32 s33, s33, 0
	s_add_u32 s34, s34, s54
	s_addc_u32 s35, s35, 0
	s_lshl_b32 s54, s36, 1
	s_lshl_b32 s55, s37, 1
	v_mul_lo_u32 v98, v222, s54
	v_mul_lo_u32 v222, v222, s55
	v_add_u32_e32 v223, v223, v222
	v_sub_u32_e32 v222, v223, v222
	v_add_u32_e32 v222, v222, v98
	v_and_b32_e32 v98, 15, v0
	v_lshrrev_b32_e32 v94, 1, v0
	v_and_b32_e32 v94, 64, v94
	v_or_b32_e32 v94, v94, v98
	v_lshlrev_b32_e32 v94, 7, v94
	v_lshlrev_b32_e32 v95, 7, v0
	v_and_b32_e32 v95, 0x2780, v95
	v_bfe_u32 v96, v0, 4, 2
	v_and_b32_e32 v97, 7, v0
	v_xor_b32_e32 v96, v96, v97
	v_lshlrev_b32_e32 v96, 4, v96
	v_xor_b32_e32 v97, 64, v96
	v_add_u32_e32 v98, v94, v97
	v_add_u32_e32 v97, v95, v97
	v_add_u32_e32 v94, v94, v96
	v_add_u32_e32 v95, v95, v96
	v_mov_b32_e32 v96, v98
	s_mov_b64 s[50:51], s[28:29]
	s_mov_b32 m0, s44
	s_nop 0
	global_load_lds_dwordx4 v222, s[50:51]
	s_mov_b64 s[52:53], s[32:33]
	s_add_u32 m0, s44, 0x4000
	s_nop 0
	global_load_lds_dwordx4 v223, s[52:53]
	s_mov_b64 s[50:51], s[30:31]
	s_add_u32 m0, s44, 0x8000
	s_nop 0
	global_load_lds_dwordx4 v222, s[50:51]
	s_mov_b64 s[52:53], s[34:35]
	s_add_u32 m0, s44, 0xc000
	s_nop 0
	global_load_lds_dwordx4 v223, s[52:53]
	s_add_u32 s50, s28, s38
	s_addc_u32 s51, s29, 0
	s_add_u32 m0, s44, 0x1000
	s_nop 0
	global_load_lds_dwordx4 v222, s[50:51]
	s_add_u32 s52, s32, s41
	s_addc_u32 s53, s33, 0
	s_add_u32 m0, s44, 0x5000
	s_nop 0
	global_load_lds_dwordx4 v223, s[52:53]
	s_add_u32 s50, s30, s38
	s_addc_u32 s51, s31, 0
	s_add_u32 m0, s44, 0x9000
	s_nop 0
	global_load_lds_dwordx4 v222, s[50:51]
	s_add_u32 s52, s34, s41
	s_addc_u32 s53, s35, 0
	s_add_u32 m0, s44, 0xd000
	s_nop 0
	global_load_lds_dwordx4 v223, s[52:53]
	s_add_u32 s50, s28, s39
	s_addc_u32 s51, s29, 0
	s_add_u32 m0, s44, 0x2000
	s_nop 0
	global_load_lds_dwordx4 v222, s[50:51]
	s_add_u32 s52, s32, s42
	s_addc_u32 s53, s33, 0
	s_add_u32 m0, s44, 0x6000
	s_nop 0
	global_load_lds_dwordx4 v223, s[52:53]
	s_add_u32 s50, s30, s39
	s_addc_u32 s51, s31, 0
	s_add_u32 m0, s44, 0xa000
	s_nop 0
	global_load_lds_dwordx4 v222, s[50:51]
	s_add_u32 s52, s34, s42
	s_addc_u32 s53, s35, 0
	s_add_u32 m0, s44, 0xe000
	s_nop 0
	global_load_lds_dwordx4 v223, s[52:53]
	s_add_u32 s50, s28, s40
	s_addc_u32 s51, s29, 0
	s_add_u32 m0, s44, 0x3000
	s_nop 0
	global_load_lds_dwordx4 v222, s[50:51]
	s_add_u32 s52, s32, s43
	s_addc_u32 s53, s33, 0
	s_add_u32 m0, s44, 0x7000
	s_nop 0
	global_load_lds_dwordx4 v223, s[52:53]
	s_add_u32 s50, s30, s40
	s_addc_u32 s51, s31, 0
	s_add_u32 m0, s44, 0xb000
	s_nop 0
	global_load_lds_dwordx4 v222, s[50:51]
	s_add_u32 s52, s34, s43
	s_addc_u32 s53, s35, 0
	s_add_u32 m0, s44, 0xf000
	s_nop 0
	global_load_lds_dwordx4 v223, s[52:53]
	.p2alignl 6, 3212836864

.LBB6_5:
	s_load_dwordx2 s[4:5], s[0:1], 0x58
	v_mov_b32_e32 v5, 0
	s_lshl_b32 s14, s3, 7
	s_lshl_b32 s15, s2, 7
	v_and_b32_e32 v75, 15, v0
	v_and_b32_e32 v77, 64, v2
	v_lshlrev_b32_e32 v76, 7, v0
	s_andn2_b64 vcc, exec, s[8:9]
	v_mov_b32_e32 v4, v5
	v_mov_b32_e32 v3, v5
	v_mov_b32_e32 v2, v5
	v_mov_b32_e32 v9, v5
	v_mov_b32_e32 v8, v5
	v_mov_b32_e32 v7, v5
	v_mov_b32_e32 v6, v5
	v_mov_b32_e32 v13, v5
	v_mov_b32_e32 v12, v5
	v_mov_b32_e32 v11, v5
	v_mov_b32_e32 v10, v5
	v_mov_b32_e32 v17, v5
	v_mov_b32_e32 v16, v5
	v_mov_b32_e32 v15, v5
	v_mov_b32_e32 v14, v5
	v_mov_b32_e32 v65, v5
	v_mov_b32_e32 v64, v5
	v_mov_b32_e32 v63, v5
	v_mov_b32_e32 v62, v5
	v_mov_b32_e32 v61, v5
	v_mov_b32_e32 v60, v5
	v_mov_b32_e32 v59, v5
	v_mov_b32_e32 v58, v5
	v_mov_b32_e32 v57, v5
	v_mov_b32_e32 v56, v5
	v_mov_b32_e32 v55, v5
	v_mov_b32_e32 v54, v5
	v_mov_b32_e32 v53, v5
	v_mov_b32_e32 v52, v5
	v_mov_b32_e32 v51, v5
	v_mov_b32_e32 v50, v5
	v_mov_b32_e32 v49, v5
	v_mov_b32_e32 v48, v5
	v_mov_b32_e32 v47, v5
	v_mov_b32_e32 v46, v5
	v_mov_b32_e32 v45, v5
	v_mov_b32_e32 v44, v5
	v_mov_b32_e32 v43, v5
	v_mov_b32_e32 v42, v5
	v_mov_b32_e32 v41, v5
	v_mov_b32_e32 v40, v5
	v_mov_b32_e32 v39, v5
	v_mov_b32_e32 v38, v5
	v_mov_b32_e32 v37, v5
	v_mov_b32_e32 v36, v5
	v_mov_b32_e32 v35, v5
	v_mov_b32_e32 v34, v5
	v_mov_b32_e32 v33, v5
	v_mov_b32_e32 v32, v5
	v_mov_b32_e32 v31, v5
	v_mov_b32_e32 v30, v5
	v_mov_b32_e32 v29, v5
	v_mov_b32_e32 v28, v5
	v_mov_b32_e32 v27, v5
	v_mov_b32_e32 v26, v5
	v_mov_b32_e32 v25, v5
	v_mov_b32_e32 v24, v5
	v_mov_b32_e32 v23, v5
	v_mov_b32_e32 v22, v5
	v_mov_b32_e32 v21, v5
	v_mov_b32_e32 v20, v5
	v_mov_b32_e32 v19, v5
	v_mov_b32_e32 v18, v5
	s_cbranch_vccnz .LBB6_9
	s_mov_b32 s49, 0
	s_load_dword s36, s[0:1], 0x10
	s_load_dwordx4 s[28:31], s[0:1], 0x0
	s_load_dwordx4 s[32:35], s[0:1], 0x30
	s_load_dwordx2 s[46:47], s[0:1], 0x40
	s_mov_b32 s37, s6
	s_lshr_b32 s45, s6, 6
	s_mul_i32 s48, s49, s45
	s_lshl_b32 s48, s48, 7
	v_lshrrev_b32_e32 v98, 6, v0
	v_lshlrev_b32_e32 v98, 10, v98
	v_lshrrev_b32_e32 v222, 3, v0
	v_readfirstlane_b32 s44, v98
	v_and_b32_e32 v223, 7, v0
	v_and_b32_e32 v98, 7, v222
	v_xor_b32_e32 v223, v223, v98
	v_lshlrev_b32_e32 v223, 4, v223
	s_waitcnt lgkmcnt(0)
	s_lshl_b32 s38, s36, 6
	s_lshl_b32 s39, s36, 7
	s_add_u32 s40, s38, s39
	s_lshl_b32 s41, s37, 6
	s_lshl_b32 s42, s37, 7
	s_add_u32 s43, s41, s42
	s_mul_i32 s54, s14, s36
	s_lshl_b32 s54, s54, 1
	s_add_u32 s54, s54, s48
	s_add_u32 s28, s28, s54
	s_addc_u32 s29, s29, 0
	s_add_u32 s30, s30, s54
	s_addc_u32 s31, s31, 0
	s_mul_i32 s54, s49, s46
	s_mul_i32 s55, s15, s37
	s_add_u32 s54, s54, s55
	s_lshl_b32 s54, s54, 1
	s_add_u32 s54, s54, s48
	s_add_u32 s32, s32, s54
	s_addc_u32 s33, s33, 0
	s_add_u32 s34, s34, s54
	s_addc_u32 s35, s35, 0
	s_lshl_b32 s54, s36, 1
	s_lshl_b32 s55, s37, 1
	v_mul_lo_u32 v98, v222, s54
	v_mul_lo_u32 v222, v222, s55
	v_add_u32_e32 v223, v223, v222
	v_sub_u32_e32 v222, v223, v222
	v_add_u32_e32 v222, v222, v98
	v_and_b32_e32 v98, 15, v0
	v_lshrrev_b32_e32 v94, 1, v0
	v_and_b32_e32 v94, 64, v94
	v_or_b32_e32 v94, v94, v98
	v_lshlrev_b32_e32 v94, 7, v94
	v_lshlrev_b32_e32 v95, 7, v0
	v_and_b32_e32 v95, 0x2780, v95
	v_bfe_u32 v96, v0, 4, 2
	v_and_b32_e32 v97, 7, v0
	v_xor_b32_e32 v96, v96, v97
	v_lshlrev_b32_e32 v96, 4, v96
	v_xor_b32_e32 v97, 64, v96
	v_add_u32_e32 v98, v94, v97
	v_add_u32_e32 v97, v95, v97
	v_add_u32_e32 v94, v94, v96
	v_add_u32_e32 v95, v95, v96
	v_mov_b32_e32 v96, v98
	v_add_u32_e32 v224, 0x10000, v94
	v_add_u32_e32 v225, 0x10000, v95
	v_add_u32_e32 v226, 0x10000, v96
	v_add_u32_e32 v227, 0x10000, v97
	s_mov_b64 s[50:51], s[28:29]
	s_mov_b32 m0, s44
	s_nop 0
	global_load_lds_dwordx4 v222, s[50:51]
	s_mov_b64 s[52:53], s[32:33]
	s_add_u32 m0, s44, 0x4000
	s_nop 0
	global_load_lds_dwordx4 v223, s[52:53]
	s_mov_b64 s[50:51], s[30:31]
	s_add_u32 m0, s44, 0x8000
	s_nop 0
	global_load_lds_dwordx4 v222, s[50:51]
	s_mov_b64 s[52:53], s[34:35]
	s_add_u32 m0, s44, 0xc000
	s_nop 0
	global_load_lds_dwordx4 v223, s[52:53]
	s_add_u32 s50, s28, s38
	s_addc_u32 s51, s29, 0
	s_add_u32 m0, s44, 0x1000
	s_nop 0
	global_load_lds_dwordx4 v222, s[50:51]
	s_add_u32 s52, s32, s41
	s_addc_u32 s53, s33, 0
	s_add_u32 m0, s44, 0x5000
	s_nop 0
	global_load_lds_dwordx4 v223, s[52:53]
	s_add_u32 s50, s30, s38
	s_addc_u32 s51, s31, 0
	s_add_u32 m0, s44, 0x9000
	s_nop 0
	global_load_lds_dwordx4 v222, s[50:51]
	s_add_u32 s52, s34, s41
	s_addc_u32 s53, s35, 0
	s_add_u32 m0, s44, 0xd000
	s_nop 0
	global_load_lds_dwordx4 v223, s[52:53]
	s_add_u32 s50, s28, s39
	s_addc_u32 s51, s29, 0
	s_add_u32 m0, s44, 0x2000
	s_nop 0
	global_load_lds_dwordx4 v222, s[50:51]
	s_add_u32 s52, s32, s42
	s_addc_u32 s53, s33, 0
	s_add_u32 m0, s44, 0x6000
	s_nop 0
	global_load_lds_dwordx4 v223, s[52:53]
	s_add_u32 s50, s30, s39
	s_addc_u32 s51, s31, 0
	s_add_u32 m0, s44, 0xa000
	s_nop 0
	global_load_lds_dwordx4 v222, s[50:51]
	s_add_u32 s52, s34, s42
	s_addc_u32 s53, s35, 0
	s_add_u32 m0, s44, 0xe000
	s_nop 0
	global_load_lds_dwordx4 v223, s[52:53]
	s_add_u32 s50, s28, s40
	s_addc_u32 s51, s29, 0
	s_add_u32 m0, s44, 0x3000
	s_nop 0
	global_load_lds_dwordx4 v222, s[50:51]
	s_add_u32 s52, s32, s43
	s_addc_u32 s53, s33, 0
	s_add_u32 m0, s44, 0x7000
	s_nop 0
	global_load_lds_dwordx4 v223, s[52:53]
	s_add_u32 s50, s30, s40
	s_addc_u32 s51, s31, 0
	s_add_u32 m0, s44, 0xb000
	s_nop 0
	global_load_lds_dwordx4 v222, s[50:51]
	s_add_u32 s52, s34, s43
	s_addc_u32 s53, s35, 0
	s_add_u32 m0, s44, 0xf000
	s_nop 0
	global_load_lds_dwordx4 v223, s[52:53]
	.p2alignl 6, 3212836864

.LBB9_43:
	s_min_i32 s20, s19, 0x4400
	s_cmp_lt_i32 s18, s20
	s_waitcnt lgkmcnt(0)
	s_cselect_b64 s[4:5], -1, 0
	s_and_b64 s[4:5], s[2:3], s[4:5]
	s_andn2_b64 vcc, exec, s[4:5]
	s_cbranch_vccnz .LBB9_329
	s_load_dword s6, s[0:1], 0x48
	s_lshl_b32 s22, s15, 7
	v_lshrrev_b32_e32 v1, 1, v0
	v_mov_b32_e32 v5, 0
	v_and_b32_e32 v76, 15, v0
	v_bfe_u32 v75, v0, 4, 2
	v_and_b32_e32 v77, 64, v1
	v_lshlrev_b32_e32 v78, 7, v0
	v_and_b32_e32 v74, 7, v0
	s_waitcnt lgkmcnt(0)
	s_cmp_lt_i32 s6, 64
	v_mov_b32_e32 v4, v5
	v_mov_b32_e32 v3, v5
	v_mov_b32_e32 v2, v5
	v_mov_b32_e32 v9, v5
	v_mov_b32_e32 v8, v5
	v_mov_b32_e32 v7, v5
	v_mov_b32_e32 v6, v5
	v_mov_b32_e32 v13, v5
	v_mov_b32_e32 v12, v5
	v_mov_b32_e32 v11, v5
	v_mov_b32_e32 v10, v5
	v_mov_b32_e32 v17, v5
	v_mov_b32_e32 v16, v5
	v_mov_b32_e32 v15, v5
	v_mov_b32_e32 v14, v5
	v_mov_b32_e32 v65, v5
	v_mov_b32_e32 v64, v5
	v_mov_b32_e32 v63, v5
	v_mov_b32_e32 v62, v5
	v_mov_b32_e32 v61, v5
	v_mov_b32_e32 v60, v5
	v_mov_b32_e32 v59, v5
	v_mov_b32_e32 v58, v5
	v_mov_b32_e32 v57, v5
	v_mov_b32_e32 v56, v5
	v_mov_b32_e32 v55, v5
	v_mov_b32_e32 v54, v5
	v_mov_b32_e32 v53, v5
	v_mov_b32_e32 v52, v5
	v_mov_b32_e32 v51, v5
	v_mov_b32_e32 v50, v5
	v_mov_b32_e32 v49, v5
	v_mov_b32_e32 v48, v5
	v_mov_b32_e32 v47, v5
	v_mov_b32_e32 v46, v5
	v_mov_b32_e32 v45, v5
	v_mov_b32_e32 v44, v5
	v_mov_b32_e32 v43, v5
	v_mov_b32_e32 v42, v5
	v_mov_b32_e32 v41, v5
	v_mov_b32_e32 v40, v5
	v_mov_b32_e32 v39, v5
	v_mov_b32_e32 v38, v5
	v_mov_b32_e32 v37, v5
	v_mov_b32_e32 v36, v5
	v_mov_b32_e32 v35, v5
	v_mov_b32_e32 v34, v5
	v_mov_b32_e32 v33, v5
	v_mov_b32_e32 v32, v5
	v_mov_b32_e32 v31, v5
	v_mov_b32_e32 v30, v5
	v_mov_b32_e32 v29, v5
	v_mov_b32_e32 v28, v5
	v_mov_b32_e32 v27, v5
	v_mov_b32_e32 v26, v5
	v_mov_b32_e32 v25, v5
	v_mov_b32_e32 v24, v5
	v_mov_b32_e32 v23, v5
	v_mov_b32_e32 v22, v5
	v_mov_b32_e32 v21, v5
	v_mov_b32_e32 v20, v5
	v_mov_b32_e32 v19, v5
	v_mov_b32_e32 v18, v5
	s_cbranch_scc1 .LBB9_47
	s_load_dword s36, s[0:1], 0x10
	s_load_dwordx4 s[28:31], s[0:1], 0x0
	s_load_dwordx4 s[32:35], s[0:1], 0x30
	s_load_dwordx2 s[46:47], s[0:1], 0x40
	s_mov_b32 s37, s6
	s_lshr_b32 s45, s6, 6
	s_mul_i32 s48, s14, s45
	s_lshl_b32 s48, s48, 7
	v_lshrrev_b32_e32 v98, 6, v0
	v_lshlrev_b32_e32 v98, 10, v98
	v_lshrrev_b32_e32 v222, 3, v0
	v_readfirstlane_b32 s44, v98
	v_and_b32_e32 v223, 7, v0
	v_and_b32_e32 v98, 7, v222
	v_xor_b32_e32 v223, v223, v98
	v_lshlrev_b32_e32 v223, 4, v223
	s_waitcnt lgkmcnt(0)
	s_lshl_b32 s38, s36, 6
	s_lshl_b32 s39, s36, 7
	s_add_u32 s40, s38, s39
	s_lshl_b32 s41, s37, 6
	s_lshl_b32 s42, s37, 7
	s_add_u32 s43, s41, s42
	s_mul_i32 s54, s18, s36
	s_lshl_b32 s54, s54, 1
	s_add_u32 s54, s54, s48
	s_add_u32 s28, s28, s54
	s_addc_u32 s29, s29, 0
	s_add_u32 s30, s30, s54
	s_addc_u32 s31, s31, 0
	s_mul_i32 s54, s21, s46
	s_mul_i32 s55, s22, s37
	s_add_u32 s54, s54, s55
	s_lshl_b32 s54, s54, 1
	s_add_u32 s54, s54, s48
	s_add_u32 s32, s32, s54
	s_addc_u32 s33, s33, 0
	s_add_u32 s34, s34, s54
	s_addc_u32 s35, s35, 0
	s_lshl_b32 s54, s36, 1
	s_lshl_b32 s55, s37, 1
	v_mul_lo_u32 v98, v222, s54
	v_mul_lo_u32 v222, v222, s55
	v_add_u32_e32 v223, v223, v222
	v_sub_u32_e32 v222, v223, v222
	v_add_u32_e32 v222, v222, v98
	v_and_b32_e32 v98, 15, v0
	v_lshrrev_b32_e32 v94, 1, v0
	v_and_b32_e32 v94, 64, v94
	v_or_b32_e32 v94, v94, v98
	v_lshlrev_b32_e32 v94, 7, v94
	v_lshlrev_b32_e32 v95, 7, v0
	v_and_b32_e32 v95, 0x2780, v95
	v_bfe_u32 v96, v0, 4, 2
	v_and_b32_e32 v97, 7, v0
	v_xor_b32_e32 v96, v96, v97
	v_lshlrev_b32_e32 v96, 4, v96
	v_xor_b32_e32 v97, 64, v96
	v_add_u32_e32 v98, v94, v97
	v_add_u32_e32 v97, v95, v97
	v_add_u32_e32 v94, v94, v96
	v_add_u32_e32 v95, v95, v96
	v_mov_b32_e32 v96, v98
	s_mov_b64 s[50:51], s[28:29]
	s_mov_b32 m0, s44
	s_nop 0
	global_load_lds_dwordx4 v222, s[50:51]
	s_mov_b64 s[52:53], s[32:33]
	s_add_u32 m0, s44, 0x4000
	s_nop 0
	global_load_lds_dwordx4 v223, s[52:53]
	s_mov_b64 s[50:51], s[30:31]
	s_add_u32 m0, s44, 0x8000
	s_nop 0
	global_load_lds_dwordx4 v222, s[50:51]
	s_mov_b64 s[52:53], s[34:35]
	s_add_u32 m0, s44, 0xc000
	s_nop 0
	global_load_lds_dwordx4 v223, s[52:53]
	s_add_u32 s50, s28, s38
	s_addc_u32 s51, s29, 0
	s_add_u32 m0, s44, 0x1000
	s_nop 0
	global_load_lds_dwordx4 v222, s[50:51]
	s_add_u32 s52, s32, s41
	s_addc_u32 s53, s33, 0
	s_add_u32 m0, s44, 0x5000
	s_nop 0
	global_load_lds_dwordx4 v223, s[52:53]
	s_add_u32 s50, s30, s38
	s_addc_u32 s51, s31, 0
	s_add_u32 m0, s44, 0x9000
	s_nop 0
	global_load_lds_dwordx4 v222, s[50:51]
	s_add_u32 s52, s34, s41
	s_addc_u32 s53, s35, 0
	s_add_u32 m0, s44, 0xd000
	s_nop 0
	global_load_lds_dwordx4 v223, s[52:53]
	s_add_u32 s50, s28, s39
	s_addc_u32 s51, s29, 0
	s_add_u32 m0, s44, 0x2000
	s_nop 0
	global_load_lds_dwordx4 v222, s[50:51]
	s_add_u32 s52, s32, s42
	s_addc_u32 s53, s33, 0
	s_add_u32 m0, s44, 0x6000
	s_nop 0
	global_load_lds_dwordx4 v223, s[52:53]
	s_add_u32 s50, s30, s39
	s_addc_u32 s51, s31, 0
	s_add_u32 m0, s44, 0xa000
	s_nop 0
	global_load_lds_dwordx4 v222, s[50:51]
	s_add_u32 s52, s34, s42
	s_addc_u32 s53, s35, 0
	s_add_u32 m0, s44, 0xe000
	s_nop 0
	global_load_lds_dwordx4 v223, s[52:53]
	s_add_u32 s50, s28, s40
	s_addc_u32 s51, s29, 0
	s_add_u32 m0, s44, 0x3000
	s_nop 0
	global_load_lds_dwordx4 v222, s[50:51]
	s_add_u32 s52, s32, s43
	s_addc_u32 s53, s33, 0
	s_add_u32 m0, s44, 0x7000
	s_nop 0
	global_load_lds_dwordx4 v223, s[52:53]
	s_add_u32 s50, s30, s40
	s_addc_u32 s51, s31, 0
	s_add_u32 m0, s44, 0xb000
	s_nop 0
	global_load_lds_dwordx4 v222, s[50:51]
	s_add_u32 s52, s34, s43
	s_addc_u32 s53, s35, 0
	s_add_u32 m0, s44, 0xf000
	s_nop 0
	global_load_lds_dwordx4 v223, s[52:53]
	.p2alignl 6, 3212836864

.LBB10_43:
	s_min_i32 s16, s15, 0x4400
	s_cmp_lt_i32 s14, s16
	s_cselect_b64 s[4:5], -1, 0
	s_and_b64 s[4:5], s[2:3], s[4:5]
	s_andn2_b64 vcc, exec, s[4:5]
	s_cbranch_vccnz .LBB10_319
	s_waitcnt lgkmcnt(0)
	s_load_dword s10, s[0:1], 0x48
	s_lshl_b32 s18, s18, 7
	v_lshrrev_b32_e32 v1, 1, v0
	v_mov_b32_e32 v65, 0
	v_and_b32_e32 v71, 15, v0
	v_bfe_u32 v70, v0, 4, 2
	v_and_b32_e32 v72, 64, v1
	v_lshlrev_b32_e32 v74, 7, v0
	v_and_b32_e32 v73, 7, v0
	s_waitcnt lgkmcnt(0)
	s_cmp_lt_i32 s10, 64
	v_mov_b32_e32 v64, v65
	v_mov_b32_e32 v63, v65
	v_mov_b32_e32 v62, v65
	v_mov_b32_e32 v61, v65
	v_mov_b32_e32 v60, v65
	v_mov_b32_e32 v59, v65
	v_mov_b32_e32 v58, v65
	v_mov_b32_e32 v57, v65
	v_mov_b32_e32 v56, v65
	v_mov_b32_e32 v55, v65
	v_mov_b32_e32 v54, v65
	v_mov_b32_e32 v53, v65
	v_mov_b32_e32 v52, v65
	v_mov_b32_e32 v51, v65
	v_mov_b32_e32 v50, v65
	v_mov_b32_e32 v49, v65
	v_mov_b32_e32 v48, v65
	v_mov_b32_e32 v47, v65
	v_mov_b32_e32 v46, v65
	v_mov_b32_e32 v45, v65
	v_mov_b32_e32 v44, v65
	v_mov_b32_e32 v43, v65
	v_mov_b32_e32 v42, v65
	v_mov_b32_e32 v41, v65
	v_mov_b32_e32 v40, v65
	v_mov_b32_e32 v39, v65
	v_mov_b32_e32 v38, v65
	v_mov_b32_e32 v37, v65
	v_mov_b32_e32 v36, v65
	v_mov_b32_e32 v35, v65
	v_mov_b32_e32 v34, v65
	v_mov_b32_e32 v33, v65
	v_mov_b32_e32 v32, v65
	v_mov_b32_e32 v31, v65
	v_mov_b32_e32 v30, v65
	v_mov_b32_e32 v29, v65
	v_mov_b32_e32 v28, v65
	v_mov_b32_e32 v27, v65
	v_mov_b32_e32 v26, v65
	v_mov_b32_e32 v25, v65
	v_mov_b32_e32 v24, v65
	v_mov_b32_e32 v23, v65
	v_mov_b32_e32 v22, v65
	v_mov_b32_e32 v21, v65
	v_mov_b32_e32 v20, v65
	v_mov_b32_e32 v19, v65
	v_mov_b32_e32 v18, v65
	v_mov_b32_e32 v17, v65
	v_mov_b32_e32 v16, v65
	v_mov_b32_e32 v15, v65
	v_mov_b32_e32 v14, v65
	v_mov_b32_e32 v13, v65
	v_mov_b32_e32 v12, v65
	v_mov_b32_e32 v11, v65
	v_mov_b32_e32 v10, v65
	v_mov_b32_e32 v9, v65
	v_mov_b32_e32 v8, v65
	v_mov_b32_e32 v7, v65
	v_mov_b32_e32 v6, v65
	v_mov_b32_e32 v5, v65
	v_mov_b32_e32 v4, v65
	v_mov_b32_e32 v3, v65
	v_mov_b32_e32 v2, v65
	s_cbranch_scc1 .LBB10_47
	s_load_dword s36, s[0:1], 0x10
	s_load_dwordx4 s[28:31], s[0:1], 0x0
	s_load_dwordx4 s[32:35], s[0:1], 0x30
	s_load_dwordx2 s[46:47], s[0:1], 0x40
	s_mov_b32 s37, s10
	s_lshr_b32 s45, s10, 6
	s_mul_i32 s48, s19, s45
	s_lshl_b32 s48, s48, 7
	v_lshrrev_b32_e32 v86, 6, v0
	v_lshlrev_b32_e32 v86, 10, v86
	v_lshrrev_b32_e32 v146, 3, v0
	v_readfirstlane_b32 s44, v86
	v_and_b32_e32 v147, 7, v0
	v_and_b32_e32 v86, 7, v146
	v_xor_b32_e32 v147, v147, v86
	v_lshlrev_b32_e32 v147, 4, v147
	s_waitcnt lgkmcnt(0)
	s_lshl_b32 s38, s36, 6
	s_lshl_b32 s39, s36, 7
	s_add_u32 s40, s38, s39
	s_lshl_b32 s41, s37, 6
	s_lshl_b32 s42, s37, 7
	s_add_u32 s43, s41, s42
	s_mul_i32 s54, s14, s36
	s_lshl_b32 s54, s54, 1
	s_add_u32 s54, s54, s48
	s_add_u32 s28, s28, s54
	s_addc_u32 s29, s29, 0
	s_add_u32 s30, s30, s54
	s_addc_u32 s31, s31, 0
	s_mul_i32 s54, s17, s46
	s_mul_i32 s55, s18, s37
	s_add_u32 s54, s54, s55
	s_lshl_b32 s54, s54, 1
	s_add_u32 s54, s54, s48
	s_add_u32 s32, s32, s54
	s_addc_u32 s33, s33, 0
	s_add_u32 s34, s34, s54
	s_addc_u32 s35, s35, 0
	s_lshl_b32 s54, s36, 1
	s_lshl_b32 s55, s37, 1
	v_mul_lo_u32 v86, v146, s54
	v_mul_lo_u32 v146, v146, s55
	v_add_u32_e32 v147, v147, v146
	v_sub_u32_e32 v146, v147, v146
	v_add_u32_e32 v146, v146, v86
	v_and_b32_e32 v86, 15, v0
	v_lshrrev_b32_e32 v82, 1, v0
	v_and_b32_e32 v82, 64, v82
	v_or_b32_e32 v82, v82, v86
	v_lshlrev_b32_e32 v82, 7, v82
	v_lshlrev_b32_e32 v83, 7, v0
	v_and_b32_e32 v83, 0x2780, v83
	v_bfe_u32 v84, v0, 4, 2
	v_and_b32_e32 v85, 7, v0
	v_xor_b32_e32 v84, v84, v85
	v_lshlrev_b32_e32 v84, 4, v84
	v_xor_b32_e32 v85, 64, v84
	v_add_u32_e32 v86, v82, v85
	v_add_u32_e32 v85, v83, v85
	v_add_u32_e32 v82, v82, v84
	v_add_u32_e32 v83, v83, v84
	v_mov_b32_e32 v84, v86
	s_mov_b64 s[50:51], s[28:29]
	s_mov_b32 m0, s44
	s_nop 0
	global_load_lds_dwordx4 v146, s[50:51]
	s_mov_b64 s[52:53], s[32:33]
	s_add_u32 m0, s44, 0x4000
	s_nop 0
	global_load_lds_dwordx4 v147, s[52:53]
	s_add_u32 s50, s28, s38
	s_addc_u32 s51, s29, 0
	s_add_u32 m0, s44, 0x1000
	s_nop 0
	global_load_lds_dwordx4 v146, s[50:51]
	s_add_u32 s52, s32, s41
	s_addc_u32 s53, s33, 0
	s_add_u32 m0, s44, 0x5000
	s_nop 0
	global_load_lds_dwordx4 v147, s[52:53]
	s_add_u32 s50, s28, s39
	s_addc_u32 s51, s29, 0
	s_add_u32 m0, s44, 0x2000
	s_nop 0
	global_load_lds_dwordx4 v146, s[50:51]
	s_add_u32 s52, s32, s42
	s_addc_u32 s53, s33, 0
	s_add_u32 m0, s44, 0x6000
	s_nop 0
	global_load_lds_dwordx4 v147, s[52:53]
	s_add_u32 s50, s28, s40
	s_addc_u32 s51, s29, 0
	s_add_u32 m0, s44, 0x3000
	s_nop 0
	global_load_lds_dwordx4 v146, s[50:51]
	s_add_u32 s52, s32, s43
	s_addc_u32 s53, s33, 0
	s_add_u32 m0, s44, 0x7000
	s_nop 0
	global_load_lds_dwordx4 v147, s[52:53]
	.p2alignl 6, 3212836864

.LBB12_43:
	s_min_i32 s26, s24, 0x4400
	s_cmp_lt_i32 s23, s26
	s_cselect_b64 s[2:3], -1, 0
	s_and_b64 s[2:3], s[14:15], s[2:3]
	s_andn2_b64 vcc, exec, s[2:3]
	s_cbranch_vccnz .LBB12_111
	s_load_dwordx2 s[2:3], s[0:1], 0x80
	s_waitcnt lgkmcnt(0)
	s_load_dwordx4 s[4:7], s[0:1], 0x70
	s_load_dword s8, s[0:1], 0x48
	s_lshl_b32 s27, s16, 7
	v_lshrrev_b32_e32 v1, 1, v0
	v_mov_b32_e32 v5, 0
	v_and_b32_e32 v75, 15, v0
	v_bfe_u32 v74, v0, 4, 2
	v_and_b32_e32 v77, 64, v1
	v_lshlrev_b32_e32 v76, 7, v0
	s_waitcnt lgkmcnt(0)
	s_cmpk_lt_i32 s8, 0x80
	v_mov_b32_e32 v4, v5
	v_mov_b32_e32 v3, v5
	v_mov_b32_e32 v2, v5
	v_mov_b32_e32 v9, v5
	v_mov_b32_e32 v8, v5
	v_mov_b32_e32 v7, v5
	v_mov_b32_e32 v6, v5
	v_mov_b32_e32 v13, v5
	v_mov_b32_e32 v12, v5
	v_mov_b32_e32 v11, v5
	v_mov_b32_e32 v10, v5
	v_mov_b32_e32 v17, v5
	v_mov_b32_e32 v16, v5
	v_mov_b32_e32 v15, v5
	v_mov_b32_e32 v14, v5
	v_mov_b32_e32 v65, v5
	v_mov_b32_e32 v64, v5
	v_mov_b32_e32 v63, v5
	v_mov_b32_e32 v62, v5
	v_mov_b32_e32 v61, v5
	v_mov_b32_e32 v60, v5
	v_mov_b32_e32 v59, v5
	v_mov_b32_e32 v58, v5
	v_mov_b32_e32 v57, v5
	v_mov_b32_e32 v56, v5
	v_mov_b32_e32 v55, v5
	v_mov_b32_e32 v54, v5
	v_mov_b32_e32 v53, v5
	v_mov_b32_e32 v52, v5
	v_mov_b32_e32 v51, v5
	v_mov_b32_e32 v50, v5
	v_mov_b32_e32 v49, v5
	v_mov_b32_e32 v48, v5
	v_mov_b32_e32 v47, v5
	v_mov_b32_e32 v46, v5
	v_mov_b32_e32 v45, v5
	v_mov_b32_e32 v44, v5
	v_mov_b32_e32 v43, v5
	v_mov_b32_e32 v42, v5
	v_mov_b32_e32 v41, v5
	v_mov_b32_e32 v40, v5
	v_mov_b32_e32 v39, v5
	v_mov_b32_e32 v38, v5
	v_mov_b32_e32 v37, v5
	v_mov_b32_e32 v36, v5
	v_mov_b32_e32 v35, v5
	v_mov_b32_e32 v34, v5
	v_mov_b32_e32 v33, v5
	v_mov_b32_e32 v32, v5
	v_mov_b32_e32 v31, v5
	v_mov_b32_e32 v30, v5
	v_mov_b32_e32 v29, v5
	v_mov_b32_e32 v28, v5
	v_mov_b32_e32 v27, v5
	v_mov_b32_e32 v26, v5
	v_mov_b32_e32 v25, v5
	v_mov_b32_e32 v24, v5
	v_mov_b32_e32 v23, v5
	v_mov_b32_e32 v22, v5
	v_mov_b32_e32 v21, v5
	v_mov_b32_e32 v20, v5
	v_mov_b32_e32 v19, v5
	v_mov_b32_e32 v18, v5
	s_cbranch_scc1 .LBB12_47
	s_load_dword s36, s[0:1], 0x10
	s_load_dwordx4 s[28:31], s[0:1], 0x0
	s_load_dwordx4 s[32:35], s[0:1], 0x30
	s_load_dwordx2 s[46:47], s[0:1], 0x40
	s_mov_b32 s37, s8
	s_lshr_b32 s45, s8, 7
	s_mul_i32 s48, s22, s45
	s_lshl_b32 s48, s48, 7
	v_lshrrev_b32_e32 v98, 6, v0
	v_lshlrev_b32_e32 v98, 10, v98
	v_lshrrev_b32_e32 v222, 3, v0
	v_readfirstlane_b32 s44, v98
	v_and_b32_e32 v223, 7, v0
	v_and_b32_e32 v98, 7, v222
	v_xor_b32_e32 v223, v223, v98
	v_lshlrev_b32_e32 v223, 4, v223
	s_waitcnt lgkmcnt(0)
	s_lshl_b32 s38, s36, 6
	s_lshl_b32 s39, s36, 7
	s_add_u32 s40, s38, s39
	s_lshl_b32 s41, s37, 6
	s_lshl_b32 s42, s37, 7
	s_add_u32 s43, s41, s42
	s_mul_i32 s54, s23, s36
	s_lshl_b32 s54, s54, 1
	s_add_u32 s54, s54, s48
	s_add_u32 s28, s28, s54
	s_addc_u32 s29, s29, 0
	s_add_u32 s30, s30, s54
	s_addc_u32 s31, s31, 0
	s_mul_i32 s54, s25, s46
	s_mul_i32 s55, s27, s37
	s_add_u32 s54, s54, s55
	s_lshl_b32 s54, s54, 1
	s_add_u32 s54, s54, s48
	s_add_u32 s32, s32, s54
	s_addc_u32 s33, s33, 0
	s_add_u32 s34, s34, s54
	s_addc_u32 s35, s35, 0
	s_lshl_b32 s54, s36, 1
	s_lshl_b32 s55, s37, 1
	v_mul_lo_u32 v98, v222, s54
	v_mul_lo_u32 v222, v222, s55
	v_add_u32_e32 v223, v223, v222
	v_sub_u32_e32 v222, v223, v222
	v_add_u32_e32 v222, v222, v98
	v_and_b32_e32 v98, 15, v0
	v_lshrrev_b32_e32 v93, 1, v0
	v_and_b32_e32 v93, 64, v93
	v_or_b32_e32 v93, v93, v98
	v_lshlrev_b32_e32 v93, 7, v93
	v_lshlrev_b32_e32 v94, 7, v0
	v_and_b32_e32 v94, 0x2780, v94
	v_bfe_u32 v95, v0, 4, 2
	v_and_b32_e32 v96, 7, v0
	v_xor_b32_e32 v95, v95, v96
	v_lshlrev_b32_e32 v95, 4, v95
	v_xor_b32_e32 v96, 64, v95
	v_add_u32_e32 v98, v93, v96
	v_add_u32_e32 v96, v94, v96
	v_add_u32_e32 v93, v93, v95
	v_add_u32_e32 v94, v94, v95
	v_mov_b32_e32 v95, v98
	s_mov_b64 s[50:51], s[28:29]
	s_mov_b32 m0, s44
	s_nop 0
	global_load_lds_dwordx4 v222, s[50:51]
	s_mov_b64 s[52:53], s[32:33]
	s_add_u32 m0, s44, 0x4000
	s_nop 0
	global_load_lds_dwordx4 v223, s[52:53]
	s_mov_b64 s[50:51], s[30:31]
	s_add_u32 m0, s44, 0x8000
	s_nop 0
	global_load_lds_dwordx4 v222, s[50:51]
	s_mov_b64 s[52:53], s[34:35]
	s_add_u32 m0, s44, 0xc000
	s_nop 0
	global_load_lds_dwordx4 v223, s[52:53]
	s_add_u32 s50, s28, s38
	s_addc_u32 s51, s29, 0
	s_add_u32 m0, s44, 0x1000
	s_nop 0
	global_load_lds_dwordx4 v222, s[50:51]
	s_add_u32 s52, s32, s41
	s_addc_u32 s53, s33, 0
	s_add_u32 m0, s44, 0x5000
	s_nop 0
	global_load_lds_dwordx4 v223, s[52:53]
	s_add_u32 s50, s30, s38
	s_addc_u32 s51, s31, 0
	s_add_u32 m0, s44, 0x9000
	s_nop 0
	global_load_lds_dwordx4 v222, s[50:51]
	s_add_u32 s52, s34, s41
	s_addc_u32 s53, s35, 0
	s_add_u32 m0, s44, 0xd000
	s_nop 0
	global_load_lds_dwordx4 v223, s[52:53]
	s_add_u32 s50, s28, s39
	s_addc_u32 s51, s29, 0
	s_add_u32 m0, s44, 0x2000
	s_nop 0
	global_load_lds_dwordx4 v222, s[50:51]
	s_add_u32 s52, s32, s42
	s_addc_u32 s53, s33, 0
	s_add_u32 m0, s44, 0x6000
	s_nop 0
	global_load_lds_dwordx4 v223, s[52:53]
	s_add_u32 s50, s30, s39
	s_addc_u32 s51, s31, 0
	s_add_u32 m0, s44, 0xa000
	s_nop 0
	global_load_lds_dwordx4 v222, s[50:51]
	s_add_u32 s52, s34, s42
	s_addc_u32 s53, s35, 0
	s_add_u32 m0, s44, 0xe000
	s_nop 0
	global_load_lds_dwordx4 v223, s[52:53]
	s_add_u32 s50, s28, s40
	s_addc_u32 s51, s29, 0
	s_add_u32 m0, s44, 0x3000
	s_nop 0
	global_load_lds_dwordx4 v222, s[50:51]
	s_add_u32 s52, s32, s43
	s_addc_u32 s53, s33, 0
	s_add_u32 m0, s44, 0x7000
	s_nop 0
	global_load_lds_dwordx4 v223, s[52:53]
	s_add_u32 s50, s30, s40
	s_addc_u32 s51, s31, 0
	s_add_u32 m0, s44, 0xb000
	s_nop 0
	global_load_lds_dwordx4 v222, s[50:51]
	s_add_u32 s52, s34, s43
	s_addc_u32 s53, s35, 0
	s_add_u32 m0, s44, 0xf000
	s_nop 0
	global_load_lds_dwordx4 v223, s[52:53]
	.p2alignl 6, 3212836864

.LBB13_43:
	s_min_i32 s17, s15, 0x4400
	s_cmp_lt_i32 s14, s17
	s_cselect_b64 s[4:5], -1, 0
	s_and_b64 s[4:5], s[2:3], s[4:5]
	s_andn2_b64 vcc, exec, s[4:5]
	s_cbranch_vccnz .LBB13_111
	s_waitcnt lgkmcnt(0)
	s_load_dword s8, s[0:1], 0x48
	s_lshl_b32 s18, s18, 7
	v_lshrrev_b32_e32 v1, 1, v0
	v_mov_b32_e32 v65, 0
	v_and_b32_e32 v71, 15, v0
	v_bfe_u32 v70, v0, 4, 2
	v_and_b32_e32 v73, 64, v1
	v_lshlrev_b32_e32 v72, 7, v0
	s_waitcnt lgkmcnt(0)
	s_cmp_lt_i32 s8, 64
	v_mov_b32_e32 v64, v65
	v_mov_b32_e32 v63, v65
	v_mov_b32_e32 v62, v65
	v_mov_b32_e32 v61, v65
	v_mov_b32_e32 v60, v65
	v_mov_b32_e32 v59, v65
	v_mov_b32_e32 v58, v65
	v_mov_b32_e32 v57, v65
	v_mov_b32_e32 v56, v65
	v_mov_b32_e32 v55, v65
	v_mov_b32_e32 v54, v65
	v_mov_b32_e32 v53, v65
	v_mov_b32_e32 v52, v65
	v_mov_b32_e32 v51, v65
	v_mov_b32_e32 v50, v65
	v_mov_b32_e32 v49, v65
	v_mov_b32_e32 v48, v65
	v_mov_b32_e32 v47, v65
	v_mov_b32_e32 v46, v65
	v_mov_b32_e32 v45, v65
	v_mov_b32_e32 v44, v65
	v_mov_b32_e32 v43, v65
	v_mov_b32_e32 v42, v65
	v_mov_b32_e32 v41, v65
	v_mov_b32_e32 v40, v65
	v_mov_b32_e32 v39, v65
	v_mov_b32_e32 v38, v65
	v_mov_b32_e32 v37, v65
	v_mov_b32_e32 v36, v65
	v_mov_b32_e32 v35, v65
	v_mov_b32_e32 v34, v65
	v_mov_b32_e32 v33, v65
	v_mov_b32_e32 v32, v65
	v_mov_b32_e32 v31, v65
	v_mov_b32_e32 v30, v65
	v_mov_b32_e32 v29, v65
	v_mov_b32_e32 v28, v65
	v_mov_b32_e32 v27, v65
	v_mov_b32_e32 v26, v65
	v_mov_b32_e32 v25, v65
	v_mov_b32_e32 v24, v65
	v_mov_b32_e32 v23, v65
	v_mov_b32_e32 v22, v65
	v_mov_b32_e32 v21, v65
	v_mov_b32_e32 v20, v65
	v_mov_b32_e32 v19, v65
	v_mov_b32_e32 v18, v65
	v_mov_b32_e32 v17, v65
	v_mov_b32_e32 v16, v65
	v_mov_b32_e32 v15, v65
	v_mov_b32_e32 v14, v65
	v_mov_b32_e32 v13, v65
	v_mov_b32_e32 v12, v65
	v_mov_b32_e32 v11, v65
	v_mov_b32_e32 v10, v65
	v_mov_b32_e32 v9, v65
	v_mov_b32_e32 v8, v65
	v_mov_b32_e32 v7, v65
	v_mov_b32_e32 v6, v65
	v_mov_b32_e32 v5, v65
	v_mov_b32_e32 v4, v65
	v_mov_b32_e32 v3, v65
	v_mov_b32_e32 v2, v65
	s_cbranch_scc1 .LBB13_47
	s_load_dword s36, s[0:1], 0x10
	s_load_dwordx4 s[28:31], s[0:1], 0x0
	s_load_dwordx4 s[32:35], s[0:1], 0x30
	s_load_dwordx2 s[46:47], s[0:1], 0x40
	s_mov_b32 s37, s8
	s_lshr_b32 s45, s8, 6
	s_mul_i32 s48, s19, s45
	s_lshl_b32 s48, s48, 7
	v_lshrrev_b32_e32 v86, 6, v0
	v_lshlrev_b32_e32 v86, 10, v86
	v_lshrrev_b32_e32 v118, 3, v0
	v_readfirstlane_b32 s44, v86
	v_and_b32_e32 v119, 7, v0
	v_and_b32_e32 v86, 7, v118
	v_xor_b32_e32 v119, v119, v86
	v_lshlrev_b32_e32 v119, 4, v119
	s_waitcnt lgkmcnt(0)
	s_lshl_b32 s38, s36, 6
	s_lshl_b32 s39, s36, 7
	s_add_u32 s40, s38, s39
	s_lshl_b32 s41, s37, 6
	s_lshl_b32 s42, s37, 7
	s_add_u32 s43, s41, s42
	s_mul_i32 s54, s14, s36
	s_lshl_b32 s54, s54, 1
	s_add_u32 s54, s54, s48
	s_add_u32 s28, s28, s54
	s_addc_u32 s29, s29, 0
	s_add_u32 s30, s30, s54
	s_addc_u32 s31, s31, 0
	s_mul_i32 s54, s16, s46
	s_mul_i32 s55, s18, s37
	s_add_u32 s54, s54, s55
	s_lshl_b32 s54, s54, 1
	s_add_u32 s54, s54, s48
	s_add_u32 s32, s32, s54
	s_addc_u32 s33, s33, 0
	s_add_u32 s34, s34, s54
	s_addc_u32 s35, s35, 0
	s_lshl_b32 s54, s36, 1
	s_lshl_b32 s55, s37, 1
	v_mul_lo_u32 v86, v118, s54
	v_mul_lo_u32 v118, v118, s55
	v_add_u32_e32 v119, v119, v118
	v_sub_u32_e32 v118, v119, v118
	v_add_u32_e32 v118, v118, v86
	v_and_b32_e32 v86, 15, v0
	v_lshrrev_b32_e32 v81, 1, v0
	v_and_b32_e32 v81, 64, v81
	v_or_b32_e32 v81, v81, v86
	v_lshlrev_b32_e32 v81, 7, v81
	v_lshlrev_b32_e32 v82, 7, v0
	v_and_b32_e32 v82, 0x2780, v82
	v_bfe_u32 v83, v0, 4, 2
	v_and_b32_e32 v84, 7, v0
	v_xor_b32_e32 v83, v83, v84
	v_lshlrev_b32_e32 v83, 4, v83
	v_xor_b32_e32 v84, 64, v83
	v_add_u32_e32 v86, v81, v84
	v_add_u32_e32 v84, v82, v84
	v_add_u32_e32 v81, v81, v83
	v_add_u32_e32 v82, v82, v83
	v_mov_b32_e32 v83, v86
	s_mov_b64 s[50:51], s[28:29]
	s_mov_b32 m0, s44
	s_nop 0
	global_load_lds_dwordx4 v118, s[50:51]
	s_mov_b64 s[52:53], s[32:33]
	s_add_u32 m0, s44, 0x4000
	s_nop 0
	global_load_lds_dwordx4 v119, s[52:53]
	s_add_u32 s50, s28, s38
	s_addc_u32 s51, s29, 0
	s_add_u32 m0, s44, 0x1000
	s_nop 0
	global_load_lds_dwordx4 v118, s[50:51]
	s_add_u32 s52, s32, s41
	s_addc_u32 s53, s33, 0
	s_add_u32 m0, s44, 0x5000
	s_nop 0
	global_load_lds_dwordx4 v119, s[52:53]
	s_add_u32 s50, s28, s39
	s_addc_u32 s51, s29, 0
	s_add_u32 m0, s44, 0x2000
	s_nop 0
	global_load_lds_dwordx4 v118, s[50:51]
	s_add_u32 s52, s32, s42
	s_addc_u32 s53, s33, 0
	s_add_u32 m0, s44, 0x6000
	s_nop 0
	global_load_lds_dwordx4 v119, s[52:53]
	s_add_u32 s50, s28, s40
	s_addc_u32 s51, s29, 0
	s_add_u32 m0, s44, 0x3000
	s_nop 0
	global_load_lds_dwordx4 v118, s[50:51]
	s_add_u32 s52, s32, s43
	s_addc_u32 s53, s33, 0
	s_add_u32 m0, s44, 0x7000
	s_nop 0
	global_load_lds_dwordx4 v119, s[52:53]
	.p2alignl 6, 3212836864
